# baseline (speedup 1.0000x reference)
.LBB2_16:
	v_add_u32_e32 v110, 0, v195
	v_add_u32_e32 v118, 0, v196
	ds_read_b128 v[82:85], v193 offset:8192
	ds_read_b128 v[86:89], v193 offset:9216
	ds_read_b128 v[90:93], v110 offset:16384
	ds_read_b128 v[98:101], v110 offset:18432
	ds_read_b128 v[94:97], v118 offset:16384
	ds_read_b128 v[102:105], v118 offset:18432
	ds_read_b128 v[106:109], v110 offset:20480
	ds_read_b128 v[114:117], v110 offset:22528
	ds_read_b128 v[110:113], v118 offset:20480
	ds_read_b128 v[118:121], v118 offset:22528
	s_waitcnt lgkmcnt(5)
	v_mfma_f32_32x32x64_f8f6f4 v[50:65], v[82:89], v[90:97], v[50:65]
	s_cmp_lg_u32 s39, 0
	s_cselect_b64 s[0:1], -1, 0
	v_cmp_eq_u32_e32 vcc, 0, v198
	s_and_b64 s[6:7], vcc, s[0:1]
	s_waitcnt lgkmcnt(4)
	v_mfma_f32_32x32x64_f8f6f4 v[34:49], v[82:89], v[98:105], v[34:49]
	s_waitcnt lgkmcnt(1)
	v_mfma_f32_32x32x64_f8f6f4 v[18:33], v[82:89], v[106:113], v[18:33]
	s_waitcnt lgkmcnt(0)
	v_mfma_f32_32x32x64_f8f6f4 v[2:17], v[82:89], v[114:121], v[2:17]
	s_and_saveexec_b64 s[0:1], s[6:7]
	s_add_i32 s6, 0, 0x1cc00
	v_mov_b32_e32 v82, 1
	v_mov_b32_e32 v83, s6
	ds_write_b32 v83, v82
	s_or_b64 exec, exec, s[0:1]
	v_mov_b32_e32 v67, v66
	s_lshl_b32 s0, s34, 9
	s_lshl_b32 s1, s33, 2
	s_add_i32 s0, s0, 0x1c000
	v_permlane32_swap_b32_e32 v67, v66
	s_add_i32 s0, s0, s1
	v_lshl_add_u32 v68, v1, 2, s0
	v_add_f32_e32 v66, v66, v67
	ds_write_b32 v68, v66
	s_add_i32 s1, s1, 0x1c000
	v_lshl_add_u32 v69, v183, 4, s1
	s_add_i32 s0, 0, 0x1cc00
	v_mov_b32_e32 v82, s0
	s_waitcnt vmcnt(0) lgkmcnt(0)
	s_barrier
	ds_read_b32 v82, v82
	s_waitcnt lgkmcnt(0)
	v_cmp_eq_u32_e32 vcc, 0, v82
	s_cbranch_vccnz .Lat_lsum
	s_mov_b32 m0, s36
	s_barrier
	global_load_lds_dwordx4 v[174:175], off
	s_mov_b32 m0, s35
	s_lshl_b32 s0, s34, 5
	global_load_lds_dwordx4 v[176:177], off
	s_mov_b32 m0, s31
	s_lshl_b32 s1, s34, 7
	global_load_lds_dwordx4 v[178:179], off
	s_mov_b32 m0, s37
	s_add_i32 s1, s1, 0
	global_load_lds_dwordx4 v[180:181], off
	v_or_b32_e32 v2, s0, v1
	s_add_i32 s1, s1, 0x1c400
	v_bitop3_b32 v4, s0, 32, v1 bitop3:0x36
	v_lshlrev_b32_e32 v2, 2, v2
	v_add_u32_e32 v3, s1, v199
	v_lshlrev_b32_e32 v5, 4, v183
	v_lshlrev_b32_e32 v4, 2, v4
	v_add3_u32 v120, s38, v2, v199
	v_mov_b32_e32 v2, 0
	s_mov_b32 s20, 0
	v_lshl_add_u32 v118, v1, 2, v3
	v_add3_u32 v119, s38, v4, v199
	v_mov_b32_e32 v101, 0xf149f2ca
	s_mov_b64 s[0:1], 0
	s_mov_b64 s[6:7], 0x4000
	s_mov_b64 s[8:9], 0x6000
	v_add_u32_e32 v121, v3, v5
	s_mov_b32 s21, 0xbdb8aa3b
	v_mov_b32_e32 v82, 0x4b400000
	v_mov_b32_e32 v100, 0x38383838
	v_mov_b32_e32 v3, v2
	v_mov_b32_e32 v4, v2
	v_mov_b32_e32 v5, v2
	v_mov_b32_e32 v6, v2
	v_mov_b32_e32 v7, v2
	v_mov_b32_e32 v8, v2
	v_mov_b32_e32 v9, v2
	v_mov_b32_e32 v10, v2
	v_mov_b32_e32 v11, v2
	v_mov_b32_e32 v12, v2
	v_mov_b32_e32 v13, v2
	v_mov_b32_e32 v14, v2
	v_mov_b32_e32 v15, v2
	v_mov_b32_e32 v16, v2
	v_mov_b32_e32 v17, v2
	v_mov_b32_e32 v18, v2
	v_mov_b32_e32 v19, v2
	v_mov_b32_e32 v20, v2
	v_mov_b32_e32 v21, v2
	v_mov_b32_e32 v22, v2
	v_mov_b32_e32 v23, v2
	v_mov_b32_e32 v24, v2
	v_mov_b32_e32 v25, v2
	v_mov_b32_e32 v26, v2
	v_mov_b32_e32 v27, v2
	v_mov_b32_e32 v28, v2
	v_mov_b32_e32 v29, v2
	v_mov_b32_e32 v30, v2
	v_mov_b32_e32 v31, v2
	v_mov_b32_e32 v32, v2
	v_mov_b32_e32 v33, v2
	v_mov_b32_e32 v34, v2
	v_mov_b32_e32 v35, v2
	v_mov_b32_e32 v36, v2
	v_mov_b32_e32 v37, v2
	v_mov_b32_e32 v38, v2
	v_mov_b32_e32 v39, v2
	v_mov_b32_e32 v40, v2
	v_mov_b32_e32 v41, v2
	v_mov_b32_e32 v42, v2
	v_mov_b32_e32 v43, v2
	v_mov_b32_e32 v44, v2
	v_mov_b32_e32 v45, v2
	v_mov_b32_e32 v46, v2
	v_mov_b32_e32 v47, v2
	v_mov_b32_e32 v48, v2
	v_mov_b32_e32 v49, v2
	v_mov_b32_e32 v50, v2
	v_mov_b32_e32 v51, v2
	v_mov_b32_e32 v52, v2
	v_mov_b32_e32 v53, v2
	v_mov_b32_e32 v54, v2
	v_mov_b32_e32 v55, v2
	v_mov_b32_e32 v56, v2
	v_mov_b32_e32 v57, v2
	v_mov_b32_e32 v58, v2
	v_mov_b32_e32 v59, v2
	v_mov_b32_e32 v60, v2
	v_mov_b32_e32 v61, v2
	v_mov_b32_e32 v62, v2
	v_mov_b32_e32 v63, v2
	v_mov_b32_e32 v64, v2
	v_mov_b32_e32 v65, v2
	v_mov_b32_e32 v66, v2
	v_mov_b32_e32 v67, v2
	v_mov_b32_e32 v68, v2
	v_mov_b32_e32 v69, v2
	v_mov_b32_e32 v70, v2
	v_mov_b32_e32 v71, v2
	v_mov_b32_e32 v72, v2
	v_mov_b32_e32 v73, v2
	v_mov_b32_e32 v74, v2
	v_mov_b32_e32 v75, v2
	v_mov_b32_e32 v76, v2
	v_mov_b32_e32 v77, v2
	v_mov_b32_e32 v78, v2
	v_mov_b32_e32 v79, v2
	v_mov_b32_e32 v80, v2
	v_mov_b32_e32 v81, v2
	s_waitcnt vmcnt(0) lgkmcnt(0)
	s_barrier
	s_cmp_eq_u32 s0, 0x7c000
	s_movk_i32 s22, 0x4000
	s_cbranch_scc1 .LBB2_21
